# LN2 (layer 1): final f32 output stores issued write-through (sc0 sc1 nt) so less L2 write-back remains at kernel end
# speedup vs baseline: 1.0030x; 1.0030x over previous
; #define LAS __attribute__((address_space(3)))
; __device__ __forceinline__ void peer_ln2_phase(LAS unsigned char* lds, int wave, int blk, const bf16* __restrict__ X1B, const bf16* __restrict__ YT, const float* __restrict__ g2, const float* __restrict__ b2, ...
;     ...
;     for (int i = 0; i < 8; ++i) {
;         const int tk = wave * 8 + i; const size_t t = (size_t)blk * 64 + tk;
;         float z[16]; float s = 0.f;
; #pragma unroll
;         for (int k = 0; k < 16; ++k) { const float xv = __uint_as_float((unsigned)__builtin_nontemporal_load((const unsigned short*)X1B + t * 1024 + lane + 64 * k) << 16); const unsigned yb = *(const LAS unsigned short*)(lds + (lane + 64 * k) * 136 + tk * 2);
;             z[k] = 1.41421356237309515f * xv + __uint_as_float(yb << 16); s += z[k]; }
; #pragma unroll
;         for (int o = 1; o < 64; o <<= 1) s += __shfl_xor(s, o);
;         const float mean = s * (1.0f / 1024.0f); float sq = 0.f;
; #pragma unroll
;         for (int k = 0; k < 16; ++k) { z[k] -= mean; sq += z[k] * z[k]; }
; #pragma unroll
;         for (int o = 1; o < 64; o <<= 1) sq += __shfl_xor(sq, o);
.LBB0_2023:
	global_load_ushort v60, v[0:1], off offset:-1024 nt
	global_load_ushort v61, v[0:1], off offset:-896 nt
	global_load_ushort v62, v[0:1], off offset:-768 nt
	s_waitcnt lgkmcnt(0)
	global_load_ushort v63, v[0:1], off offset:-640 nt
	global_load_ushort v64, v[0:1], off offset:-512 nt
	global_load_ushort v65, v[0:1], off offset:-384 nt
	global_load_ushort v66, v[0:1], off offset:-256 nt
	global_load_ushort v67, v[0:1], off offset:-128 nt
	global_load_ushort v68, v[0:1], off nt
	global_load_ushort v69, v[0:1], off offset:128 nt
	global_load_ushort v70, v[0:1], off offset:256 nt
	global_load_ushort v71, v[0:1], off offset:384 nt
	global_load_ushort v72, v[0:1], off offset:512 nt
	global_load_ushort v73, v[0:1], off offset:640 nt
	global_load_ushort v74, v[0:1], off offset:768 nt
	global_load_ushort v75, v[0:1], off offset:896 nt
	v_add_u32_e32 v52, 0xffffbc00, v43
	v_add_u32_e32 v46, 0xfffef000, v43
	v_add_u32_e32 v47, 0xffff1200, v43
	v_add_u32_e32 v48, 0xffff3400, v43
	v_add_u32_e32 v49, 0xffff5600, v43
	v_add_u32_e32 v50, 0xffff7800, v43
	v_add_u32_e32 v51, 0xffff9a00, v43
	v_add_u32_e32 v53, 0xffffde00, v43
	ds_read_u16 v54, v43
	ds_read_u16 v55, v43 offset:8704
	ds_read_u16 v56, v43 offset:17408
	ds_read_u16 v57, v43 offset:26112
	ds_read_u16 v58, v43 offset:34816
	ds_read_u16 v59, v43 offset:43520
	ds_read_u16 v76, v43 offset:52224
	ds_read_u16 v77, v43 offset:60928
	ds_read_u16 v78, v46
	ds_read_u16 v79, v47
	ds_read_u16 v80, v48
	ds_read_u16 v81, v49
	ds_read_u16 v82, v50
	ds_read_u16 v83, v51
	ds_read_u16 v52, v52
	ds_read_u16 v84, v53
	s_waitcnt lgkmcnt(10)
	v_lshlrev_b32_e32 v46, 16, v59
	s_waitcnt lgkmcnt(7)
	v_lshlrev_b32_e32 v59, 16, v78
	v_lshlrev_b32_e32 v47, 16, v58
	s_waitcnt lgkmcnt(6)
	v_lshlrev_b32_e32 v58, 16, v79
	v_lshlrev_b32_e32 v48, 16, v57
	s_waitcnt lgkmcnt(5)
	v_lshlrev_b32_e32 v57, 16, v80
	v_lshlrev_b32_e32 v49, 16, v56
	s_waitcnt lgkmcnt(4)
	v_lshlrev_b32_e32 v56, 16, v81
	v_lshlrev_b32_e32 v50, 16, v55
	s_waitcnt lgkmcnt(3)
	v_lshlrev_b32_e32 v55, 16, v82
	v_lshlrev_b32_e32 v51, 16, v54
	s_waitcnt lgkmcnt(2)
	v_lshlrev_b32_e32 v54, 16, v83
	s_waitcnt lgkmcnt(1)
	v_lshlrev_b32_e32 v53, 16, v52
	s_waitcnt lgkmcnt(0)
	v_lshlrev_b32_e32 v52, 16, v84
	s_andn2_b64 vcc, exec, s[6:7]
	s_waitcnt vmcnt(15)
	v_lshlrev_b32_e32 v60, 16, v60
	s_waitcnt vmcnt(14)
	v_lshlrev_b32_e32 v61, 16, v61
	v_fmac_f32_e32 v59, 0x3fb504f3, v60
	s_waitcnt vmcnt(13)
	v_lshlrev_b32_e32 v62, 16, v62
	v_fmac_f32_e32 v58, 0x3fb504f3, v61
	v_add_f32_e32 v60, 0, v59
	s_waitcnt vmcnt(12)
	v_lshlrev_b32_e32 v63, 16, v63
	v_fmac_f32_e32 v57, 0x3fb504f3, v62
	v_add_f32_e32 v60, v60, v58
	s_waitcnt vmcnt(11)
	v_lshlrev_b32_e32 v64, 16, v64
	v_fmac_f32_e32 v56, 0x3fb504f3, v63
	v_add_f32_e32 v60, v60, v57
	s_waitcnt vmcnt(10)
	v_lshlrev_b32_e32 v65, 16, v65
	v_fmac_f32_e32 v55, 0x3fb504f3, v64
	v_add_f32_e32 v60, v60, v56
	s_waitcnt vmcnt(9)
	v_lshlrev_b32_e32 v66, 16, v66
	v_fmac_f32_e32 v54, 0x3fb504f3, v65
	v_add_f32_e32 v60, v60, v55
	s_waitcnt vmcnt(8)
	v_lshlrev_b32_e32 v67, 16, v67
	v_fmac_f32_e32 v53, 0x3fb504f3, v66
	v_add_f32_e32 v60, v60, v54
	s_waitcnt vmcnt(7)
	v_lshlrev_b32_e32 v68, 16, v68
	v_fmac_f32_e32 v52, 0x3fb504f3, v67
	v_add_f32_e32 v60, v60, v53
	s_waitcnt vmcnt(6)
	v_lshlrev_b32_e32 v69, 16, v69
	v_fmac_f32_e32 v51, 0x3fb504f3, v68
	v_add_f32_e32 v60, v60, v52
	s_waitcnt vmcnt(5)
	v_lshlrev_b32_e32 v70, 16, v70
	v_fmac_f32_e32 v50, 0x3fb504f3, v69
	v_add_f32_e32 v60, v60, v51
	s_waitcnt vmcnt(4)
	v_lshlrev_b32_e32 v71, 16, v71
	v_fmac_f32_e32 v49, 0x3fb504f3, v70
	v_add_f32_e32 v60, v60, v50
	s_waitcnt vmcnt(3)
	v_lshlrev_b32_e32 v72, 16, v72
	v_fmac_f32_e32 v48, 0x3fb504f3, v71
	v_add_f32_e32 v60, v60, v49
	s_waitcnt vmcnt(2)
	v_lshlrev_b32_e32 v73, 16, v73
	v_fmac_f32_e32 v47, 0x3fb504f3, v72
	v_add_f32_e32 v60, v60, v48
	v_fmac_f32_e32 v46, 0x3fb504f3, v73
	v_add_f32_e32 v60, v60, v47
	v_add_f32_e32 v61, v60, v46
	s_waitcnt vmcnt(1)
	v_lshlrev_b32_e32 v62, 16, v74
	v_lshlrev_b32_e32 v60, 16, v76
	v_fmac_f32_e32 v60, 0x3fb504f3, v62
	v_add_f32_e32 v62, v61, v60
	s_waitcnt vmcnt(0)
	v_lshlrev_b32_e32 v63, 16, v75
	v_lshlrev_b32_e32 v61, 16, v77
	v_fmac_f32_e32 v61, 0x3fb504f3, v63
	v_add_f32_e32 v62, v62, v61
	s_nop 1
	v_add_f32_dpp v62, v62, v62 row_shr:1 row_mask:0xf bank_mask:0xf
	s_nop 1
	v_add_f32_dpp v62, v62, v62 row_shr:2 row_mask:0xf bank_mask:0xf
	s_nop 1
	v_add_f32_dpp v62, v62, v62 row_shr:4 row_mask:0xf bank_mask:0xf
	s_nop 1
	v_add_f32_dpp v62, v62, v62 row_shr:8 row_mask:0xf bank_mask:0xf
	s_nop 1
	v_add_f32_dpp v62, v62, v62 row_bcast:15 row_mask:0xa bank_mask:0xf
	s_nop 1
	v_add_f32_dpp v62, v62, v62 row_bcast:31 row_mask:0xc bank_mask:0xf
	s_nop 1
	v_readlane_b32 s98, v62, 63
	s_nop 1
	v_mov_b32_e32 v62, s98
	v_fmac_f32_e32 v58, 0xba800000, v62
	v_fmac_f32_e32 v59, 0xba800000, v62
	v_mul_f32_e32 v63, v58, v58
	v_fmac_f32_e32 v57, 0xba800000, v62
	v_fmac_f32_e32 v63, v59, v59
	v_fmac_f32_e32 v56, 0xba800000, v62
	v_fmac_f32_e32 v63, v57, v57
	v_fmac_f32_e32 v55, 0xba800000, v62
	v_fmac_f32_e32 v63, v56, v56
	v_fmac_f32_e32 v54, 0xba800000, v62
	v_fmac_f32_e32 v63, v55, v55
	v_fmac_f32_e32 v53, 0xba800000, v62
	v_fmac_f32_e32 v63, v54, v54
	v_fmac_f32_e32 v52, 0xba800000, v62
	v_fmac_f32_e32 v63, v53, v53
	v_fmac_f32_e32 v51, 0xba800000, v62
	v_fmac_f32_e32 v63, v52, v52
	v_fmac_f32_e32 v50, 0xba800000, v62
	v_fmac_f32_e32 v63, v51, v51
	v_fmac_f32_e32 v49, 0xba800000, v62
	v_fmac_f32_e32 v63, v50, v50
	v_fmac_f32_e32 v48, 0xba800000, v62
	v_fmac_f32_e32 v63, v49, v49
	v_fmac_f32_e32 v47, 0xba800000, v62
	v_fmac_f32_e32 v63, v48, v48
	v_fmac_f32_e32 v46, 0xba800000, v62
	v_fmac_f32_e32 v63, v47, v47
	v_fmac_f32_e32 v60, 0xba800000, v62
	v_fmac_f32_e32 v63, v46, v46
	v_fmac_f32_e32 v63, v60, v60
	v_fmac_f32_e32 v61, 0xba800000, v62
	v_fmac_f32_e32 v63, v61, v61
	ds_bpermute_b32 v62, v37, v63
	s_waitcnt lgkmcnt(0)
	v_add_f32_e32 v62, v63, v62
	ds_bpermute_b32 v63, v38, v62
	s_waitcnt lgkmcnt(0)
	v_add_f32_e32 v62, v62, v63
	ds_bpermute_b32 v63, v39, v62
	s_waitcnt lgkmcnt(0)
	v_add_f32_e32 v62, v62, v63
	ds_bpermute_b32 v63, v40, v62
	s_waitcnt lgkmcnt(0)
	v_add_f32_e32 v62, v62, v63
	ds_bpermute_b32 v63, v41, v62
	s_waitcnt lgkmcnt(0)
	v_add_f32_e32 v62, v62, v63
	ds_bpermute_b32 v63, v42, v62
	s_cbranch_vccnz .LBB0_2022
; __device__ __forceinline__ void peer_ln2_phase(LAS unsigned char* lds, int wave, int blk, const bf16* __restrict__ X1B, const bf16* __restrict__ YT, const float* __restrict__ g2, const float* __restrict__ b2, ...
;     ...
;         for (int o = 1; o < 64; o <<= 1) sq += __shfl_xor(sq, o);
;         const float rstd = 1.0f / sqrtf(sq * (1.0f / 1024.0f) + 1e-5f);
; #pragma unroll
;         for (int k = 0; k < 16; ++k) { z[k] = z[k] * rstd * gv[k] + bv[k]; if (outf) __builtin_nontemporal_store(z[k], outf + t * 1024 + lane + 64 * k); }
	s_waitcnt lgkmcnt(0)
	v_add_f32_e32 v62, v62, v63
	v_fmamk_f32 v62, v62, 0x3a800000, v44
	v_mul_f32_e32 v63, 0x4f800000, v62
	v_cmp_gt_f32_e32 vcc, s8, v62
	s_nop 1
	v_cndmask_b32_e32 v62, v62, v63, vcc
	v_sqrt_f32_e32 v63, v62
	s_nop 0
	v_add_u32_e32 v64, -1, v63
	v_fma_f32 v66, -v64, v63, v62
	v_add_u32_e32 v65, 1, v63
	v_cmp_ge_f32_e64 s[0:1], 0, v66
	s_nop 1
	v_cndmask_b32_e64 v64, v63, v64, s[0:1]
	v_fma_f32 v63, -v65, v63, v62
	v_cmp_lt_f32_e64 s[0:1], 0, v63
	s_nop 1
	v_cndmask_b32_e64 v63, v64, v65, s[0:1]
	v_mul_f32_e32 v64, 0x37800000, v63
	v_cndmask_b32_e32 v63, v63, v64, vcc
	v_cmp_class_f32_e32 vcc, v62, v45
	s_nop 1
	v_cndmask_b32_e32 v64, v63, v62, vcc
	v_div_scale_f32 v65, s[0:1], v64, v64, 1.0
	v_rcp_f32_e32 v66, v65
	v_lshl_add_u64 v[62:63], v[2:3], 0, s[4:5]
	v_fma_f32 v67, -v65, v66, 1.0
	v_fmac_f32_e32 v66, v67, v66
	v_div_scale_f32 v67, vcc, 1.0, v64, 1.0
	v_mul_f32_e32 v68, v67, v66
	v_fma_f32 v69, -v65, v68, v67
	v_fmac_f32_e32 v68, v69, v66
	v_fma_f32 v65, -v65, v68, v67
	v_div_fmas_f32 v65, v65, v66, v68
	v_div_fixup_f32 v64, v65, v64, 1.0
	v_mul_f32_e32 v46, v46, v64
	v_fma_f32 v46, v26, v46, v34
	global_store_dword v[62:63], v46, off offset:3328 sc0 sc1 nt
	v_mul_f32_e32 v46, v60, v64
	v_fma_f32 v46, v27, v46, v35
	v_mul_f32_e32 v59, v59, v64
	v_mul_f32_e32 v58, v58, v64
	v_mul_f32_e32 v57, v57, v64
	v_mul_f32_e32 v56, v56, v64
	v_mul_f32_e32 v55, v55, v64
	v_mul_f32_e32 v54, v54, v64
	v_mul_f32_e32 v53, v53, v64
	v_mul_f32_e32 v52, v52, v64
	v_mul_f32_e32 v51, v51, v64
	v_mul_f32_e32 v50, v50, v64
	v_mul_f32_e32 v49, v49, v64
	v_mul_f32_e32 v48, v48, v64
	v_mul_f32_e32 v47, v47, v64
	global_store_dword v[62:63], v46, off offset:3584 sc0 sc1 nt
	v_mul_f32_e32 v46, v61, v64
	v_fma_f32 v59, v21, v59, v29
	v_fma_f32 v58, v4, v58, v13
	v_fma_f32 v57, v5, v57, v14
	v_fma_f32 v56, v6, v56, v15
	v_fma_f32 v55, v7, v55, v16
	v_fma_f32 v54, v9, v54, v17
	v_fma_f32 v53, v10, v53, v18
	v_fma_f32 v52, v11, v52, v19
	v_fma_f32 v51, v12, v51, v20
	v_fma_f32 v50, v22, v50, v30
	v_fma_f32 v49, v23, v49, v31
	v_fma_f32 v48, v24, v48, v32
	v_fma_f32 v47, v25, v47, v33
	v_fma_f32 v46, v28, v46, v36
	global_store_dword v[62:63], v59, off sc0 sc1 nt
	global_store_dword v[62:63], v58, off offset:256 sc0 sc1 nt
	global_store_dword v[62:63], v57, off offset:512 sc0 sc1 nt
	global_store_dword v[62:63], v56, off offset:768 sc0 sc1 nt
	global_store_dword v[62:63], v55, off offset:1024 sc0 sc1 nt
	global_store_dword v[62:63], v54, off offset:1280 sc0 sc1 nt
	global_store_dword v[62:63], v53, off offset:1536 sc0 sc1 nt
	global_store_dword v[62:63], v52, off offset:1792 sc0 sc1 nt
	global_store_dword v[62:63], v51, off offset:2048 sc0 sc1 nt
	global_store_dword v[62:63], v50, off offset:2304 sc0 sc1 nt
	global_store_dword v[62:63], v49, off offset:2560 sc0 sc1 nt
	global_store_dword v[62:63], v48, off offset:2816 sc0 sc1 nt
	global_store_dword v[62:63], v47, off offset:3072 sc0 sc1 nt
	global_store_dword v[62:63], v46, off offset:3840 sc0 sc1 nt
	s_branch .LBB0_2022
